# baseline (speedup 1.0000x reference)
_Z8pam_mainPKDv4_jS1_S1_PKfS3_PDF16_Pf:
	s_load_dwordx8 s[4:11], s[0:1], 0x0
	s_load_dwordx4 s[12:15], s[0:1], 0x20
	s_load_dwordx2 s[16:17], s[0:1], 0x30
	v_and_b32_e32 v1, 63, v0
	v_lshrrev_b32_e32 v3, 6, v0
	v_lshlrev_b32_e32 v2, 4, v1
	v_lshlrev_b32_e32 v4, 2, v1
	v_readfirstlane_b32 s18, v3
	v_and_b32_e32 v3, 31, v1
	v_lshlrev_b32_e32 v5, 2, v3
	s_mul_i32 s19, s2, 54
	s_mul_i32 s20, s2, 3
	s_lshr_b32 s20, s20, 4
	s_mul_i32 s21, s20, 0x120
	s_sub_u32 s21, s19, s21
	s_cmp_ge_u32 s20, 24
	s_cselect_b32 s22, 0x120, 0
	s_add_u32 s22, s22, s21
	s_add_u32 s23, s20, 1
	s_cmp_ge_u32 s23, 24
	s_cselect_b32 s24, 0x120, 0
	s_sub_u32 s25, 0x120, s21
	s_cmp_lt_u32 s25, 54
	s_cselect_b32 s26, 1, 0
	s_mul_i32 s25, s25, 43
	s_lshr_b32 s25, s25, 8
	s_cmp_eq_u32 s26, 1
	s_cselect_b32 s25, s25, 100
	s_mov_b32 s29, s2
	s_mov_b32 s46, 0
	s_mov_b32 s47, 30720
	s_mov_b32 s48, 61440
	s_mov_b32 s27, 0
	s_mov_b32 s28, 1
	s_mul_i32 s30, s18, 0xd00
	s_add_u32 s30, s30, 92160
	v_add_u32_e32 v7, s30, v2
	v_mul_u32_u24_e32 v6, 0x68, v3
	v_lshrrev_b32_e32 v130, 2, v1
	v_and_b32_e32 v130, 8, v130
	v_add3_u32 v6, v6, v130, s30
	v_mov_b32_e32 v150, 0xf149f2ca
	s_cmp_ge_u32 s18, 8
	s_cbranch_scc0 .Lm_noprio
	s_setprio 1
.Lm_noprio:
	s_waitcnt lgkmcnt(0)
	s_sub_u32 s30, s27, s25
	s_mul_i32 s30, s30, 6
	s_add_u32 s30, s30, s24
	s_mul_i32 s31, s27, 6
	s_add_u32 s31, s31, s22
	s_cmp_lt_u32 s27, s25
	s_cselect_b32 s30, s31, s30
	s_lshl_b32 s33, s18, 10
	s_lshl_b32 s31, s30, 12
	s_add_u32 s31, s31, s33
	s_add_u32 s50, s8, s31
	s_addc_u32 s51, s9, 0
	s_add_u32 s52, s50, 0x3000
	s_addc_u32 s53, s51, 0
	s_add_u32 s34, s46, s33
	s_mov_b32 m0, s34
	s_add_u32 s35, s34, 0x3000
	global_load_lds_dwordx4 v2, s[50:51]
	s_mov_b32 m0, s35
	s_nop 0
	global_load_lds_dwordx4 v2, s[52:53]
	s_cmp_lt_u32 s18, 6
	s_cbranch_scc0 .Lm_nok_p0
	s_lshl_b32 s31, s30, 10
	s_add_u32 s31, s31, s33
	s_add_u32 s54, s4, s31
	s_addc_u32 s55, s5, 0
	s_add_u32 s34, s34, 24576
	s_mov_b32 m0, s34
	s_nop 0
	global_load_lds_dwordx4 v2, s[54:55]
